# speedup vs baseline: 1.0942x; 1.0042x over previous
.LBB3_12:
	s_or_b64 exec, exec, s[2:3]
	v_lshlrev_b32_e32 v28, 2, v1
	s_waitcnt lgkmcnt(0)
	global_load_dword v32, v28, s[16:17]
	global_load_dword v31, v28, s[18:19]
	s_movk_i32 s38, 0xff94
	s_movk_i32 s39, 0xffee
	s_add_i32 s40, s22, -4
	v_mov_b32_e32 v131, 0x7f
	v_mov_b32_e32 v132, 0x7c
	v_min_u32_e32 v133, 27, v50
	v_min_u32_e32 v134, 3, v48
	v_or_b32_e32 v134, 24, v134
	v_lshl_or_b32 v128, v48, 6, v1
	v_mul_u32_u24_e32 v129, 0x25f, v128
	v_lshrrev_b32_e32 v129, 16, v129
	v_mad_i32_i24 v128, v129, s38, v128
	v_mul_u32_u24_e32 v130, 0xe39, v128
	v_lshrrev_b32_e32 v130, 16, v130
	v_mad_i32_i24 v128, v130, s39, v128
	v_add_u32_e32 v130, s25, v130
	v_med3_i32 v130, v130, 0, v131
	v_lshl_add_u32 v128, v128, 2, s40
	v_med3_i32 v128, v128, 0, v132
	v_min_u32_e32 v129, 15, v129
	v_lshlrev_b32_e32 v129, 14, v129
	v_lshlrev_b32_e32 v130, 7, v130
	v_or3_b32 v94, v130, v129, v128
	v_lshl_or_b32 v128, v49, 6, v1
	v_mul_u32_u24_e32 v129, 0x25f, v128
	v_lshrrev_b32_e32 v129, 16, v129
	v_mad_i32_i24 v128, v129, s38, v128
	v_mul_u32_u24_e32 v130, 0xe39, v128
	v_lshrrev_b32_e32 v130, 16, v130
	v_mad_i32_i24 v128, v130, s39, v128
	v_add_u32_e32 v130, s25, v130
	v_med3_i32 v130, v130, 0, v131
	v_lshl_add_u32 v128, v128, 2, s40
	v_med3_i32 v128, v128, 0, v132
	v_min_u32_e32 v129, 15, v129
	v_lshlrev_b32_e32 v129, 14, v129
	v_lshlrev_b32_e32 v130, 7, v130
	v_or3_b32 v96, v130, v129, v128
	v_lshl_or_b32 v128, v133, 6, v1
	v_mul_u32_u24_e32 v129, 0x25f, v128
	v_lshrrev_b32_e32 v129, 16, v129
	v_mad_i32_i24 v128, v129, s38, v128
	v_mul_u32_u24_e32 v130, 0xe39, v128
	v_lshrrev_b32_e32 v130, 16, v130
	v_mad_i32_i24 v128, v130, s39, v128
	v_add_u32_e32 v130, s25, v130
	v_med3_i32 v130, v130, 0, v131
	v_lshl_add_u32 v128, v128, 2, s40
	v_med3_i32 v128, v128, 0, v132
	v_min_u32_e32 v129, 15, v129
	v_lshlrev_b32_e32 v129, 14, v129
	v_lshlrev_b32_e32 v130, 7, v130
	v_or3_b32 v98, v130, v129, v128
	v_lshl_or_b32 v128, v134, 6, v1
	v_mul_u32_u24_e32 v129, 0x25f, v128
	v_lshrrev_b32_e32 v129, 16, v129
	v_mad_i32_i24 v128, v129, s38, v128
	v_mul_u32_u24_e32 v130, 0xe39, v128
	v_lshrrev_b32_e32 v130, 16, v130
	v_mad_i32_i24 v128, v130, s39, v128
	v_add_u32_e32 v130, s25, v130
	v_med3_i32 v130, v130, 0, v131
	v_lshl_add_u32 v128, v128, 2, s40
	v_med3_i32 v128, v128, 0, v132
	v_min_u32_e32 v129, 15, v129
	v_lshlrev_b32_e32 v129, 14, v129
	v_lshlrev_b32_e32 v130, 7, v130
	v_or3_b32 v100, v130, v129, v128
	v_cmp_eq_u32_e32 vcc, 27, v134
	v_readfirstlane_b32 s41, v100
	s_nop 1
	v_mov_b32_e32 v135, s41
	v_cndmask_b32_e32 v100, v100, v135, vcc
	v_accvgpr_write_b32 a3, 0
	v_accvgpr_write_b32 a2, 0
	v_accvgpr_write_b32 a1, 0
	v_accvgpr_write_b32 a0, 0
	v_accvgpr_write_b32 a7, 0
	v_accvgpr_write_b32 a6, 0
	v_accvgpr_write_b32 a5, 0
	v_accvgpr_write_b32 a4, 0
	v_accvgpr_write_b32 a15, 0
	v_accvgpr_write_b32 a14, 0
	v_accvgpr_write_b32 a13, 0
	v_accvgpr_write_b32 a12, 0
	v_accvgpr_write_b32 a19, 0
	v_accvgpr_write_b32 a18, 0
	v_accvgpr_write_b32 a17, 0
	v_accvgpr_write_b32 a16, 0
	v_accvgpr_write_b32 a31, 0
	v_accvgpr_write_b32 a30, 0
	v_accvgpr_write_b32 a29, 0
	v_accvgpr_write_b32 a28, 0
	v_accvgpr_write_b32 a63, 0
	v_accvgpr_write_b32 a62, 0
	v_accvgpr_write_b32 a61, 0
	v_accvgpr_write_b32 a60, 0
	v_accvgpr_write_b32 a11, 0
	v_accvgpr_write_b32 a10, 0
	v_accvgpr_write_b32 a9, 0
	v_accvgpr_write_b32 a8, 0
	v_accvgpr_write_b32 a23, 0
	v_accvgpr_write_b32 a22, 0
	v_accvgpr_write_b32 a21, 0
	v_accvgpr_write_b32 a20, 0
	v_accvgpr_write_b32 a27, 0
	v_accvgpr_write_b32 a26, 0
	v_accvgpr_write_b32 a25, 0
	v_accvgpr_write_b32 a24, 0
	v_accvgpr_write_b32 a39, 0
	v_accvgpr_write_b32 a38, 0
	v_accvgpr_write_b32 a37, 0
	v_accvgpr_write_b32 a36, 0
	v_accvgpr_write_b32 a47, 0
	v_accvgpr_write_b32 a46, 0
	v_accvgpr_write_b32 a45, 0
	v_accvgpr_write_b32 a44, 0
	v_accvgpr_write_b32 a67, 0
	v_accvgpr_write_b32 a66, 0
	v_accvgpr_write_b32 a65, 0
	v_accvgpr_write_b32 a64, 0
	v_accvgpr_write_b32 a35, 0
	v_accvgpr_write_b32 a34, 0
	v_accvgpr_write_b32 a33, 0
	v_accvgpr_write_b32 a32, 0
	v_accvgpr_write_b32 a43, 0
	v_accvgpr_write_b32 a42, 0
	v_accvgpr_write_b32 a41, 0
	v_accvgpr_write_b32 a40, 0
	v_accvgpr_write_b32 a51, 0
	v_accvgpr_write_b32 a50, 0
	v_accvgpr_write_b32 a49, 0
	v_accvgpr_write_b32 a48, 0
	v_accvgpr_write_b32 a55, 0
	v_accvgpr_write_b32 a54, 0
	v_accvgpr_write_b32 a53, 0
	v_accvgpr_write_b32 a52, 0
	v_accvgpr_write_b32 a59, 0
	v_accvgpr_write_b32 a58, 0
	v_accvgpr_write_b32 a57, 0
	v_accvgpr_write_b32 a56, 0
	v_accvgpr_write_b32 a71, 0
	v_accvgpr_write_b32 a70, 0
	v_accvgpr_write_b32 a69, 0
	v_accvgpr_write_b32 a68, 0
	s_waitcnt vmcnt(0)
	v_mov_b32_dpp v28, v26 row_shr:1 row_mask:0xf bank_mask:0xf bound_ctrl:1
	v_mov_b32_dpp v29, v27 row_shr:1 row_mask:0xf bank_mask:0xf bound_ctrl:1
	v_pk_add_f32 v[26:27], v[26:27], v[28:29]
	v_mov_b32_e32 v34, 0
	v_mov_b32_e32 v35, 0
	v_mov_b32_dpp v28, v26 row_shr:2 row_mask:0xf bank_mask:0xf bound_ctrl:1
	v_mov_b32_dpp v29, v27 row_shr:2 row_mask:0xf bank_mask:0xf bound_ctrl:1
	v_pk_add_f32 v[26:27], v[26:27], v[28:29]
	v_cmp_eq_u32_e32 vcc, 63, v1
	s_nop 0
	v_mov_b32_dpp v28, v26 row_shr:4 row_mask:0xf bank_mask:0xf bound_ctrl:1
	v_mov_b32_dpp v29, v27 row_shr:4 row_mask:0xf bank_mask:0xf bound_ctrl:1
	v_pk_add_f32 v[26:27], v[26:27], v[28:29]
	s_nop 1
	v_mov_b32_dpp v28, v26 row_shr:8 row_mask:0xf bank_mask:0xf bound_ctrl:1
	v_mov_b32_dpp v29, v27 row_shr:8 row_mask:0xf bank_mask:0xf bound_ctrl:1
	v_pk_add_f32 v[28:29], v[26:27], v[28:29]
	v_mov_b32_e32 v27, 0
	v_mov_b32_e32 v26, 0
	v_mov_b32_dpp v34, v28 row_bcast:15 row_mask:0xa bank_mask:0xf
	v_mov_b32_dpp v35, v29 row_bcast:15 row_mask:0xa bank_mask:0xf
	v_pk_add_f32 v[28:29], v[28:29], v[34:35]
	s_nop 1
	v_mov_b32_dpp v26, v28 row_bcast:31 row_mask:0xc bank_mask:0xf
	v_mov_b32_dpp v27, v29 row_bcast:31 row_mask:0xc bank_mask:0xf
	s_and_saveexec_b64 s[2:3], vcc
	v_lshl_add_u32 v33, v48, 3, 0
	v_add_u32_e32 v33, 0x15800, v33
	v_pk_add_f32 v[26:27], v[28:29], v[26:27]
	ds_write_b64 v33, v[26:27]
	s_or_b64 exec, exec, s[2:3]
	v_cmp_gt_u32_e32 vcc, 64, v0
	s_waitcnt lgkmcnt(0)
	s_barrier
	s_and_saveexec_b64 s[10:11], vcc
	s_cbranch_execz .LBB3_16
	s_add_i32 s2, 0, 0x15800
	v_mov_b32_e32 v26, s2
	s_add_i32 s2, 0, 0x15810
	v_mov_b32_e32 v33, s2
	ds_read_b128 v[26:29], v26
	ds_read_b128 v[34:37], v33
	s_mov_b32 s2, 0xf800000
	s_waitcnt lgkmcnt(1)
	v_add_f32_e32 v26, v26, v28
	s_waitcnt lgkmcnt(0)
	v_add_f32_e32 v28, v34, v36
	v_add_f32_e32 v26, v26, v28
	v_add_f32_e32 v27, v27, v29
	v_add_f32_e32 v28, v35, v37
	v_add_f32_e32 v27, v27, v28
	v_mul_f32_e32 v26, 0x35800000, v26
	v_mul_f32_e32 v27, 0x35800000, v27
	v_fma_f32 v27, -v26, v26, v27
	v_add_f32_e32 v27, 0x3727c5ac, v27
	v_mul_f32_e32 v28, 0x4f800000, v27
	v_cmp_gt_f32_e32 vcc, s2, v27
	s_nop 1
	v_cndmask_b32_e32 v27, v27, v28, vcc
	v_sqrt_f32_e32 v28, v27
	s_nop 0
	v_add_u32_e32 v29, -1, v28
	v_fma_f32 v33, -v29, v28, v27
	v_cmp_ge_f32_e64 s[2:3], 0, v33
	v_add_u32_e32 v33, 1, v28
	s_nop 0
	v_cndmask_b32_e64 v29, v28, v29, s[2:3]
	v_fma_f32 v28, -v33, v28, v27
	v_cmp_lt_f32_e64 s[2:3], 0, v28
	s_nop 1
	v_cndmask_b32_e64 v28, v29, v33, s[2:3]
	v_mul_f32_e32 v29, 0x37800000, v28
	v_cndmask_b32_e32 v28, v28, v29, vcc
	v_mov_b32_e32 v29, 0x260
	v_cmp_class_f32_e32 vcc, v27, v29
	s_nop 1
	v_cndmask_b32_e32 v27, v28, v27, vcc
	v_div_scale_f32 v28, s[2:3], v27, v27, 1.0
	v_rcp_f32_e32 v29, v28
	s_nop 0
	v_fma_f32 v33, -v28, v29, 1.0
	v_fmac_f32_e32 v29, v33, v29
	v_div_scale_f32 v33, vcc, 1.0, v27, 1.0
	v_mul_f32_e32 v34, v33, v29
	v_fma_f32 v35, -v28, v34, v33
	v_fmac_f32_e32 v34, v35, v29
	v_fma_f32 v28, -v28, v34, v33
	v_div_fmas_f32 v28, v28, v29, v34
	v_div_fixup_f32 v27, v28, v27, 1.0
	v_lshl_add_u32 v28, v0, 2, 0
	v_mul_f32_e32 v27, v32, v27
	v_add_u32_e32 v29, 0x15600, v28
	ds_write_b32 v29, v27
	v_fma_f32 v26, -v26, v27, v31
	v_add_u32_e32 v27, 0x15700, v28
	ds_write_b32 v27, v26

.Lk3_top:
	s_bitcmp1_b32 s19, 0
	s_cselect_b32 s14, 0x4800, 0
	v_add_u32_e32 v78, s14, v125
	s_waitcnt lgkmcnt(8)
	v_mfma_f32_16x16x32_f16 a[0:3], v[42:45], v[14:17], a[0:3]
	ds_read_b128 v[70:73], v78
	s_add_i32 s15, s19, 1
	v_mfma_f32_16x16x32_f16 a[4:7], v[42:45], v[18:21], a[4:7]
	ds_read_b128 v[66:69], v78 offset:1024
	s_mul_hi_u32 s28, s15, 0xaaaaaaab
	s_waitcnt lgkmcnt(9)
	v_mfma_f32_16x16x32_f16 a[12:15], v[38:41], v[14:17], a[12:15]
	ds_read_b128 v[58:61], v78 offset:2048
	s_lshr_b32 s28, s28, 1
	s_bitcmp1_b32 s15, 0
	s_cselect_b32 s31, 0x4800, 0
	v_mfma_f32_16x16x32_f16 a[16:19], v[38:41], v[18:21], a[16:19]
	ds_read_b128 v[54:57], v78 offset:3072
	s_mul_i32 s29, s28, 3
	v_xor_b32_e32 v82, 64, v126
	s_waitcnt lgkmcnt(10)
	v_mfma_f32_16x16x32_f16 a[28:31], v[34:37], v[14:17], a[28:31]
	ds_read_b128 v[46:49], v78 offset:4096
	s_sub_i32 s29, s15, s29
	v_xor_b32_e32 v86, 64, v127
	v_mfma_f32_16x16x32_f16 a[60:63], v[34:37], v[18:21], a[60:63]
	ds_read_b128 v[50:53], v78 offset:5120
	s_add_i32 s30, s29, 1
	v_add_lshl_u32 v128, s28, v121, 1
	s_waitcnt lgkmcnt(11)
	v_mfma_f32_16x16x32_f16 a[8:11], v[30:33], v[14:17], a[8:11]
	ds_read_b128 v[62:65], v78 offset:6144
	v_and_or_b32 v129, s29, 1, v128
	v_mfma_f32_16x16x32_f16 a[20:23], v[30:33], v[18:21], a[20:23]
	ds_read_b128 v[74:77], v78 offset:7168
	v_and_or_b32 v130, s30, 1, v128
	s_lshr_b32 s29, s29, 1
	s_lshr_b32 s30, s30, 1
	s_waitcnt lgkmcnt(12)
	v_mfma_f32_16x16x32_f16 a[24:27], v[26:29], v[14:17], a[24:27]
	ds_read_b128 v[78:81], v78 offset:8192
	v_lshl_add_u32 v129, v129, 5, v129
	v_mfma_f32_16x16x32_f16 a[36:39], v[26:29], v[18:21], a[36:39]
	ds_read_b128 v[82:85], v82
	v_lshl_add_u32 v130, v130, 5, v130
	s_waitcnt lgkmcnt(13)
	v_mfma_f32_16x16x32_f16 a[44:47], v[22:25], v[14:17], a[44:47]
	ds_read_b128 v[86:89], v86
	v_add3_u32 v129, v123, s29, v129
	v_mfma_f32_16x16x32_f16 a[64:67], v[22:25], v[18:21], a[64:67]
	v_add3_u32 v130, v123, s30, v130
	v_lshlrev_b32_e32 v128, 7, v129
	s_waitcnt lgkmcnt(13)
	v_mfma_f32_16x16x32_f16 a[32:35], v[10:13], v[14:17], a[32:35]
	v_bitop3_b32 v129, v129, v122, 7 bitop3:0x6c
	v_lshlrev_b32_e32 v136, 7, v130
	v_mfma_f32_16x16x32_f16 a[40:43], v[10:13], v[18:21], a[40:43]
	v_bitop3_b32 v130, v130, v122, 7 bitop3:0x6c
	v_lshl_or_b32 v126, v129, 4, v128
	s_waitcnt lgkmcnt(12)
	v_mfma_f32_16x16x32_f16 a[48:51], v[6:9], v[14:17], a[48:51]
	v_lshl_or_b32 v127, v130, 4, v136
	v_add_u32_e32 v131, s31, v124
	v_mfma_f32_16x16x32_f16 a[52:55], v[6:9], v[18:21], a[52:55]
	v_lshl_add_u64 v[132:133], v[116:117], 0, s[0:1]
	s_add_i32 s35, s32, s14
	s_waitcnt lgkmcnt(11)
	v_mfma_f32_16x16x32_f16 a[56:59], v[2:5], v[14:17], a[56:59]
	v_lshl_add_u64 v[134:135], v[116:117], 0, s[2:3]
	s_add_i32 s36, s33, s14
	s_add_i32 s37, s34, s14
	v_mfma_f32_16x16x32_f16 a[68:71], v[2:5], v[18:21], a[68:71]
	s_cmp_eq_u32 s19, 8
	s_waitcnt lgkmcnt(0)
	s_cbranch_scc1 .Lk3_nb
	s_waitcnt vmcnt(0)

.Lk3_h2:
	v_mfma_f32_16x16x32_f16 a[0:3], v[70:73], v[82:85], a[0:3]
	ds_read_b128 v[14:17], v126
	v_mfma_f32_16x16x32_f16 a[4:7], v[70:73], v[86:89], a[4:7]
	ds_read_b128 v[18:21], v127
	v_mfma_f32_16x16x32_f16 a[12:15], v[66:69], v[82:85], a[12:15]
	ds_read_b128 v[42:45], v131
	v_mfma_f32_16x16x32_f16 a[16:19], v[66:69], v[86:89], a[16:19]
	ds_read_b128 v[38:41], v131 offset:1024
	v_mfma_f32_16x16x32_f16 a[28:31], v[58:61], v[82:85], a[28:31]
	ds_read_b128 v[34:37], v131 offset:2048
	v_mfma_f32_16x16x32_f16 a[60:63], v[58:61], v[86:89], a[60:63]
	ds_read_b128 v[30:33], v131 offset:3072
	v_mfma_f32_16x16x32_f16 a[8:11], v[54:57], v[82:85], a[8:11]
	ds_read_b128 v[26:29], v131 offset:4096
	v_mfma_f32_16x16x32_f16 a[20:23], v[54:57], v[86:89], a[20:23]
	ds_read_b128 v[22:25], v131 offset:5120
	v_mfma_f32_16x16x32_f16 a[24:27], v[46:49], v[82:85], a[24:27]
	ds_read_b128 v[10:13], v131 offset:6144
	v_mfma_f32_16x16x32_f16 a[36:39], v[46:49], v[86:89], a[36:39]
	ds_read_b128 v[6:9], v131 offset:7168
	v_mfma_f32_16x16x32_f16 a[44:47], v[50:53], v[82:85], a[44:47]
	ds_read_b128 v[2:5], v131 offset:8192
	v_mfma_f32_16x16x32_f16 a[64:67], v[50:53], v[86:89], a[64:67]
	v_mfma_f32_16x16x32_f16 a[32:35], v[62:65], v[82:85], a[32:35]
	v_mfma_f32_16x16x32_f16 a[40:43], v[62:65], v[86:89], a[40:43]
	v_mfma_f32_16x16x32_f16 a[48:51], v[74:77], v[82:85], a[48:51]
	v_mfma_f32_16x16x32_f16 a[52:55], v[74:77], v[86:89], a[52:55]
	v_mfma_f32_16x16x32_f16 a[56:59], v[78:81], v[82:85], a[56:59]
	v_mfma_f32_16x16x32_f16 a[68:71], v[78:81], v[86:89], a[68:71]
	v_lshl_add_u64 v[116:117], v[116:117], 0, s[6:7]
	s_mov_b32 s19, s15
	s_cmp_eq_u32 s15, 9
	s_cbranch_scc0 .Lk3_top
	s_waitcnt lgkmcnt(0)

	.amdhsa_kernel _Z7kfinal3PKDF16_PKfS2_S2_PK15HIP_vector_typeIjLj4EES2_Pf
		.amdhsa_group_segment_fixed_size 0
		.amdhsa_private_segment_fixed_size 0
		.amdhsa_kernarg_size 56
		.amdhsa_user_sgpr_count 2
		.amdhsa_user_sgpr_dispatch_ptr 0
		.amdhsa_user_sgpr_queue_ptr 0
		.amdhsa_user_sgpr_kernarg_segment_ptr 1
		.amdhsa_user_sgpr_dispatch_id 0
		.amdhsa_user_sgpr_kernarg_preload_length 0
		.amdhsa_user_sgpr_kernarg_preload_offset 0
		.amdhsa_user_sgpr_private_segment_size 0
		.amdhsa_uses_dynamic_stack 0
		.amdhsa_enable_private_segment 0
		.amdhsa_system_sgpr_workgroup_id_x 1
		.amdhsa_system_sgpr_workgroup_id_y 0
		.amdhsa_system_sgpr_workgroup_id_z 0
		.amdhsa_system_sgpr_workgroup_info 0
		.amdhsa_system_vgpr_workitem_id 0
		.amdhsa_next_free_vgpr 213
		.amdhsa_next_free_sgpr 42
		.amdhsa_accum_offset 140
		.amdhsa_reserve_vcc 1
		.amdhsa_float_round_mode_32 0
		.amdhsa_float_round_mode_16_64 0
		.amdhsa_float_denorm_mode_32 3
		.amdhsa_float_denorm_mode_16_64 3
		.amdhsa_dx10_clamp 1
		.amdhsa_ieee_mode 1
		.amdhsa_fp16_overflow 0
		.amdhsa_tg_split 0
		.amdhsa_exception_fp_ieee_invalid_op 0
		.amdhsa_exception_fp_denorm_src 0
		.amdhsa_exception_fp_ieee_div_zero 0
		.amdhsa_exception_fp_ieee_overflow 0
		.amdhsa_exception_fp_ieee_underflow 0
		.amdhsa_exception_fp_ieee_inexact 0
		.amdhsa_exception_int_div_zero 0
	.end_amdhsa_kernel

amdhsa.kernels:
  - .agpr_count:     0
    .args:
      - .actual_access:  read_only
        .address_space:  global
        .offset:         0
        .size:           8
        .value_kind:     global_buffer
      - .actual_access:  read_only
        .address_space:  global
        .offset:         8
        .size:           8
        .value_kind:     global_buffer
      - .actual_access:  read_only
        .address_space:  global
        .offset:         16
        .size:           8
        .value_kind:     global_buffer
      - .actual_access:  read_only
        .address_space:  global
        .offset:         24
        .size:           8
        .value_kind:     global_buffer
      - .actual_access:  read_only
        .address_space:  global
        .offset:         32
        .size:           8
        .value_kind:     global_buffer
      - .actual_access:  read_only
        .address_space:  global
        .offset:         40
        .size:           8
        .value_kind:     global_buffer
      - .actual_access:  write_only
        .address_space:  global
        .offset:         48
        .size:           8
        .value_kind:     global_buffer
      - .actual_access:  write_only
        .address_space:  global
        .offset:         56
        .size:           8
        .value_kind:     global_buffer
      - .actual_access:  write_only
        .address_space:  global
        .offset:         64
        .size:           8
        .value_kind:     global_buffer
      - .actual_access:  write_only
        .address_space:  global
        .offset:         72
        .size:           8
        .value_kind:     global_buffer
    .group_segment_fixed_size: 12000
    .kernarg_segment_align: 8
    .kernarg_segment_size: 80
    .language:       OpenCL C
    .language_version:
      - 2
      - 0
    .max_flat_workgroup_size: 256
    .name:           _Z2k0PKfS0_S0_S0_S0_S0_PDF16_PfS1_S1_
    .private_segment_fixed_size: 0
    .sgpr_count:     24
    .sgpr_spill_count: 0
    .symbol:         _Z2k0PKfS0_S0_S0_S0_S0_PDF16_PfS1_S1_.kd
    .uniform_work_group_size: 1
    .uses_dynamic_stack: false
    .vgpr_count:     150
    .vgpr_spill_count: 0
    .wavefront_size: 64
  - .agpr_count:     16
    .args:
      - .actual_access:  read_only
        .address_space:  global
        .offset:         0
        .size:           8
        .value_kind:     global_buffer
      - .actual_access:  read_only
        .address_space:  global
        .offset:         8
        .size:           8
        .value_kind:     global_buffer
      - .actual_access:  read_only
        .address_space:  global
        .offset:         16
        .size:           8
        .value_kind:     global_buffer
      - .actual_access:  read_only
        .address_space:  global
        .offset:         24
        .size:           8
        .value_kind:     global_buffer
      - .actual_access:  read_only
        .address_space:  global
        .offset:         32
        .size:           8
        .value_kind:     global_buffer
      - .actual_access:  write_only
        .address_space:  global
        .offset:         40
        .size:           8
        .value_kind:     global_buffer
      - .actual_access:  write_only
        .address_space:  global
        .offset:         48
        .size:           8
        .value_kind:     global_buffer
    .group_segment_fixed_size: 14112
    .kernarg_segment_align: 8
    .kernarg_segment_size: 56
    .language:       OpenCL C
    .language_version:
      - 2
      - 0
    .max_flat_workgroup_size: 256
    .name:           _Z4khidPKDF16_PKfS2_S2_S0_PDF16_Pf
    .private_segment_fixed_size: 0
    .sgpr_count:     24
    .sgpr_spill_count: 0
    .symbol:         _Z4khidPKDF16_PKfS2_S2_S0_PDF16_Pf.kd
    .uniform_work_group_size: 1
    .uses_dynamic_stack: false
    .vgpr_count:     148
    .vgpr_spill_count: 0
    .wavefront_size: 64
  - .agpr_count:     144
    .args:
      - .actual_access:  read_only
        .address_space:  global
        .offset:         0
        .size:           8
        .value_kind:     global_buffer
      - .actual_access:  read_only
        .address_space:  global
        .offset:         8
        .size:           8
        .value_kind:     global_buffer
      - .actual_access:  read_only
        .address_space:  global
        .offset:         16
        .size:           8
        .value_kind:     global_buffer
      - .actual_access:  read_only
        .address_space:  global
        .offset:         24
        .size:           8
        .value_kind:     global_buffer
      - .address_space:  global
        .offset:         32
        .size:           8
        .value_kind:     global_buffer
      - .address_space:  global
        .offset:         40
        .size:           8
        .value_kind:     global_buffer
      - .address_space:  global
        .offset:         48
        .size:           8
        .value_kind:     global_buffer
    .group_segment_fixed_size: 0
    .kernarg_segment_align: 8
    .kernarg_segment_size: 56
    .language:       OpenCL C
    .language_version:
      - 2
      - 0
    .max_flat_workgroup_size: 256
    .name:           _Z6kfinalPKDF16_PKfS2_S2_PK15HIP_vector_typeIjLj4EES2_Pf
    .private_segment_fixed_size: 0
    .sgpr_count:     41
    .sgpr_spill_count: 0
    .symbol:         _Z6kfinalPKDF16_PKfS2_S2_PK15HIP_vector_typeIjLj4EES2_Pf.kd
    .uniform_work_group_size: 1
    .uses_dynamic_stack: false
    .vgpr_count:     400
    .vgpr_spill_count: 0
    .wavefront_size: 64
  - .agpr_count:     73
    .args:
      - .actual_access:  read_only
        .address_space:  global
        .offset:         0
        .size:           8
        .value_kind:     global_buffer
      - .actual_access:  read_only
        .address_space:  global
        .offset:         8
        .size:           8
        .value_kind:     global_buffer
      - .actual_access:  read_only
        .address_space:  global
        .offset:         16
        .size:           8
        .value_kind:     global_buffer
      - .actual_access:  read_only
        .address_space:  global
        .offset:         24
        .size:           8
        .value_kind:     global_buffer
      - .address_space:  global
        .offset:         32
        .size:           8
        .value_kind:     global_buffer
      - .address_space:  global
        .offset:         40
        .size:           8
        .value_kind:     global_buffer
      - .address_space:  global
        .offset:         48
        .size:           8
        .value_kind:     global_buffer
    .group_segment_fixed_size: 0
    .kernarg_segment_align: 8
    .kernarg_segment_size: 56
    .language:       OpenCL C
    .language_version:
      - 2
      - 0
    .max_flat_workgroup_size: 512
    .name:           _Z7kfinal3PKDF16_PKfS2_S2_PK15HIP_vector_typeIjLj4EES2_Pf
    .private_segment_fixed_size: 0
    .sgpr_count:     48
    .sgpr_spill_count: 0
    .symbol:         _Z7kfinal3PKDF16_PKfS2_S2_PK15HIP_vector_typeIjLj4EES2_Pf.kd
    .uniform_work_group_size: 1
    .uses_dynamic_stack: false
    .vgpr_count:     213
    .vgpr_spill_count: 0
    .wavefront_size: 64
